# grid barrier: last arriver issues buffer_inv sc1 right behind buffer_wbl2 and waits vmcnt(1) before the flag bump (all arrivers keep the agent-scope invalidate)
# baseline (speedup 1.0000x reference)
; __device__ __forceinline__ unsigned xb_ld(unsigned* p)              { return __hip_atomic_load(p, __ATOMIC_RELAXED, __HIP_MEMORY_SCOPE_AGENT); }
; __device__ __forceinline__ unsigned xb_add(unsigned* p, unsigned v) { return __hip_atomic_fetch_add(p, v, __ATOMIC_RELAXED, __HIP_MEMORY_SCOPE_AGENT); }
; #define XB_SPIN(cond, bar) do { unsigned _sp = 0; while (cond) { __builtin_amdgcn_s_sleep(1); \
;     if ((++_sp & 255u) == 0u) { if (xb_ld(&(bar)[XB_TMO])) break; if (_sp > XB_SPIN_CAP) { atomicAdd(&(bar)[XB_TMO], 1u); break; } } } } while (0)
; __device__ __forceinline__ void xcd_barrier(const XcdBarrier& b) {
;     ...
;     if (b.w0 == 0 && ln_ == 0) {
;         unsigned* bar = b.bar; unsigned one_ = 1u;
;         asm volatile("" : "+s"(bar), "+v"(one_));
;         __builtin_amdgcn_s_waitcnt(0);
;         unsigned nloc = b.st[0], nx = b.st[1];
;         if (nloc == 0u) { xcd_barrier_complete(bar, b.x, nloc, nx); b.st[0] = nloc; b.st[1] = nx; }
;         const unsigned old = xb_add(&bar[XB_XSUB(b.x)], one_);
;         const unsigned gen = old / nloc;
;         if (old + 1u == (gen + 1u) * nloc) {
;             __builtin_amdgcn_fence(__ATOMIC_RELEASE, "agent");
;             asm volatile("s_waitcnt vmcnt(0)" ::: "memory");
;             const unsigned og = xb_add(&bar[XB_TOP], one_);
;             const unsigned tg = og / nx;
;             if (og + 1u == (tg + 1u) * nx) xb_add(&bar[XB_TOPGEN], one_);
;             else XB_SPIN(xb_ld(&bar[XB_TOPGEN]) == tg, bar);
;             __builtin_amdgcn_fence(__ATOMIC_ACQUIRE, "agent");
;             xb_add(&bar[XB_XGEN(b.x)], one_);
;             asm volatile("s_waitcnt vmcnt(0)" ::: "memory");
;         } else {
;             XB_SPIN(xb_ld(&bar[XB_XGEN(b.x)]) == gen, bar);
;             __builtin_amdgcn_fence(__ATOMIC_ACQUIRE, "agent");
;             asm volatile("s_waitcnt vmcnt(0)" ::: "memory");
;         }
.LBB0_142:
	s_lshl_b32 s2, s33, 8
	s_add_u32 s23, s34, s2
	s_addc_u32 s22, s35, 0
	v_mov_b32_e32 v1, s23
	v_add_co_u32_e32 v4, vcc, 0x1000, v1
	v_mov_b32_e32 v1, s22
	s_nop 0
	v_addc_co_u32_e32 v5, vcc, 0, v1, vcc
	flat_atomic_add v1, v[4:5], v10 offset:1024 sc0
	v_cvt_f32_u32_e32 v3, v2
	v_sub_u32_e32 v4, 0, v2
	v_rcp_iflag_f32_e32 v3, v3
	s_nop 0
	v_mul_f32_e32 v3, 0x4f7ffffe, v3
	v_cvt_u32_f32_e32 v3, v3
	v_mul_lo_u32 v4, v4, v3
	v_mul_hi_u32 v4, v3, v4
	v_add_u32_e32 v3, v3, v4
	s_waitcnt vmcnt(0) lgkmcnt(0)
	v_mul_hi_u32 v3, v1, v3
	v_mul_lo_u32 v5, v3, v2
	v_add_u32_e32 v4, 1, v1
	v_sub_u32_e32 v1, v1, v5
	v_add_u32_e32 v6, 1, v3
	v_cmp_ge_u32_e32 vcc, v1, v2
	v_sub_u32_e32 v5, v1, v2
	s_nop 0
	v_cndmask_b32_e32 v3, v3, v6, vcc
	v_cndmask_b32_e32 v1, v1, v5, vcc
	v_add_u32_e32 v5, 1, v3
	v_cmp_ge_u32_e32 vcc, v1, v2
	s_nop 1
	v_cndmask_b32_e32 v1, v3, v5, vcc
	v_mad_u64_u32 v[2:3], s[2:3], v2, v1, v[2:3]
	v_cmp_ne_u32_e32 vcc, v4, v2
	v_mov_b32_e32 v20, 0
	s_cbranch_vccnz .Lxbar0_nl
	buffer_wbl2 sc1
	buffer_inv sc1
	s_waitcnt vmcnt(1)
	s_sub_u32 s2, s23, s34
	s_lshr_b32 s2, s2, 6
	s_add_u32 s6, s34, 0x2400
	s_addc_u32 s7, s35, 0
	s_add_u32 s6, s6, s2
	s_addc_u32 s7, s7, 0
	global_atomic_add v20, v10, s[6:7]
	s_branch .Lxbar0_poll

; __device__ __forceinline__ unsigned xb_ld(unsigned* p)              { return __hip_atomic_load(p, __ATOMIC_RELAXED, __HIP_MEMORY_SCOPE_AGENT); }
; __device__ __forceinline__ unsigned xb_add(unsigned* p, unsigned v) { return __hip_atomic_fetch_add(p, v, __ATOMIC_RELAXED, __HIP_MEMORY_SCOPE_AGENT); }
; #define XB_SPIN(cond, bar) do { unsigned _sp = 0; while (cond) { __builtin_amdgcn_s_sleep(1); \
;     if ((++_sp & 255u) == 0u) { if (xb_ld(&(bar)[XB_TMO])) break; if (_sp > XB_SPIN_CAP) { atomicAdd(&(bar)[XB_TMO], 1u); break; } } } } while (0)
; __device__ __forceinline__ void xcd_barrier(const XcdBarrier& b) {
;     ...
;     if (b.w0 == 0 && ln_ == 0) {
;         unsigned* bar = b.bar; unsigned one_ = 1u;
;         asm volatile("" : "+s"(bar), "+v"(one_));
;         __builtin_amdgcn_s_waitcnt(0);
;         unsigned nloc = b.st[0], nx = b.st[1];
;         if (nloc == 0u) { xcd_barrier_complete(bar, b.x, nloc, nx); b.st[0] = nloc; b.st[1] = nx; }
;         const unsigned old = xb_add(&bar[XB_XSUB(b.x)], one_);
;         const unsigned gen = old / nloc;
;         if (old + 1u == (gen + 1u) * nloc) {
;             __builtin_amdgcn_fence(__ATOMIC_RELEASE, "agent");
;             asm volatile("s_waitcnt vmcnt(0)" ::: "memory");
;             const unsigned og = xb_add(&bar[XB_TOP], one_);
;             const unsigned tg = og / nx;
;             if (og + 1u == (tg + 1u) * nx) xb_add(&bar[XB_TOPGEN], one_);
;             else XB_SPIN(xb_ld(&bar[XB_TOPGEN]) == tg, bar);
;             __builtin_amdgcn_fence(__ATOMIC_ACQUIRE, "agent");
;             xb_add(&bar[XB_XGEN(b.x)], one_);
;             asm volatile("s_waitcnt vmcnt(0)" ::: "memory");
;         } else {
;             XB_SPIN(xb_ld(&bar[XB_XGEN(b.x)]) == gen, bar);
;             __builtin_amdgcn_fence(__ATOMIC_ACQUIRE, "agent");
;             asm volatile("s_waitcnt vmcnt(0)" ::: "memory");
;         }
.LBB0_430:
	v_readlane_b32 s4, v253, 57
	s_lshl_b32 s4, s4, 2
	s_add_u32 s25, s2, s4
	s_addc_u32 s24, s3, 0
	v_mov_b32_e32 v3, s25
	v_add_co_u32_e32 v6, vcc, 0x1000, v3
	v_mov_b32_e32 v3, s24
	s_nop 0
	v_addc_co_u32_e32 v7, vcc, 0, v3, vcc
	flat_atomic_add v5, v[6:7], v1 offset:1024 sc0
	v_cvt_f32_u32_e32 v3, v4
	v_sub_u32_e32 v6, 0, v4
	v_rcp_iflag_f32_e32 v3, v3
	s_nop 0
	v_mul_f32_e32 v3, 0x4f7ffffe, v3
	v_cvt_u32_f32_e32 v3, v3
	v_mul_lo_u32 v6, v6, v3
	v_mul_hi_u32 v6, v3, v6
	v_add_u32_e32 v3, v3, v6
	s_waitcnt vmcnt(0) lgkmcnt(0)
	v_mul_hi_u32 v3, v5, v3
	v_mul_lo_u32 v6, v3, v4
	v_sub_u32_e32 v6, v5, v6
	v_cmp_ge_u32_e32 vcc, v6, v4
	v_add_u32_e32 v7, 1, v3
	s_nop 0
	v_cndmask_b32_e32 v3, v3, v7, vcc
	v_sub_u32_e32 v7, v6, v4
	v_cndmask_b32_e32 v6, v6, v7, vcc
	v_cmp_ge_u32_e32 vcc, v6, v4
	v_add_u32_e32 v6, 1, v3
	s_nop 0
	v_cndmask_b32_e32 v3, v3, v6, vcc
	v_add_u32_e32 v6, 1, v5
	v_mad_u64_u32 v[4:5], s[4:5], v4, v3, v[4:5]
	v_cmp_ne_u32_e32 vcc, v6, v4
	v_mov_b32_e32 v20, 0
	s_cbranch_vccnz .Lxbar1_nl
	buffer_wbl2 sc1
	buffer_inv sc1
	s_waitcnt vmcnt(1)
	s_sub_u32 s4, s25, s2
	s_lshr_b32 s4, s4, 6
	s_add_u32 s8, s2, 0x2400
	s_addc_u32 s9, s3, 0
	s_add_u32 s8, s8, s4
	s_addc_u32 s9, s9, 0
	global_atomic_add v20, v1, s[8:9]
	s_branch .Lxbar1_poll

; __device__ __forceinline__ unsigned xb_ld(unsigned* p)              { return __hip_atomic_load(p, __ATOMIC_RELAXED, __HIP_MEMORY_SCOPE_AGENT); }
; __device__ __forceinline__ unsigned xb_add(unsigned* p, unsigned v) { return __hip_atomic_fetch_add(p, v, __ATOMIC_RELAXED, __HIP_MEMORY_SCOPE_AGENT); }
; #define XB_SPIN(cond, bar) do { unsigned _sp = 0; while (cond) { __builtin_amdgcn_s_sleep(1); \
;     if ((++_sp & 255u) == 0u) { if (xb_ld(&(bar)[XB_TMO])) break; if (_sp > XB_SPIN_CAP) { atomicAdd(&(bar)[XB_TMO], 1u); break; } } } } while (0)
; __device__ __forceinline__ void xcd_barrier(const XcdBarrier& b) {
;     ...
;     if (b.w0 == 0 && ln_ == 0) {
;         unsigned* bar = b.bar; unsigned one_ = 1u;
;         asm volatile("" : "+s"(bar), "+v"(one_));
;         __builtin_amdgcn_s_waitcnt(0);
;         unsigned nloc = b.st[0], nx = b.st[1];
;         if (nloc == 0u) { xcd_barrier_complete(bar, b.x, nloc, nx); b.st[0] = nloc; b.st[1] = nx; }
;         const unsigned old = xb_add(&bar[XB_XSUB(b.x)], one_);
;         const unsigned gen = old / nloc;
;         if (old + 1u == (gen + 1u) * nloc) {
;             __builtin_amdgcn_fence(__ATOMIC_RELEASE, "agent");
;             asm volatile("s_waitcnt vmcnt(0)" ::: "memory");
;             const unsigned og = xb_add(&bar[XB_TOP], one_);
;             const unsigned tg = og / nx;
;             if (og + 1u == (tg + 1u) * nx) xb_add(&bar[XB_TOPGEN], one_);
;             else XB_SPIN(xb_ld(&bar[XB_TOPGEN]) == tg, bar);
;             __builtin_amdgcn_fence(__ATOMIC_ACQUIRE, "agent");
;             xb_add(&bar[XB_XGEN(b.x)], one_);
;             asm volatile("s_waitcnt vmcnt(0)" ::: "memory");
;         } else {
;             XB_SPIN(xb_ld(&bar[XB_XGEN(b.x)]) == gen, bar);
;             __builtin_amdgcn_fence(__ATOMIC_ACQUIRE, "agent");
;             asm volatile("s_waitcnt vmcnt(0)" ::: "memory");
;         }
.LBB0_681:
	v_readlane_b32 s6, v253, 57
	s_lshl_b32 s6, s6, 2
	s_add_u32 s27, s4, s6
	s_addc_u32 s26, s5, 0
	v_mov_b32_e32 v3, s27
	v_add_co_u32_e32 v6, vcc, 0x1000, v3
	v_mov_b32_e32 v3, s26
	s_nop 0
	v_addc_co_u32_e32 v7, vcc, 0, v3, vcc
	flat_atomic_add v5, v[6:7], v1 offset:1024 sc0
	v_cvt_f32_u32_e32 v3, v4
	v_sub_u32_e32 v6, 0, v4
	v_rcp_iflag_f32_e32 v3, v3
	s_nop 0
	v_mul_f32_e32 v3, 0x4f7ffffe, v3
	v_cvt_u32_f32_e32 v3, v3
	v_mul_lo_u32 v6, v6, v3
	v_mul_hi_u32 v6, v3, v6
	v_add_u32_e32 v3, v3, v6
	s_waitcnt vmcnt(0) lgkmcnt(0)
	v_mul_hi_u32 v3, v5, v3
	v_mul_lo_u32 v6, v3, v4
	v_sub_u32_e32 v6, v5, v6
	v_cmp_ge_u32_e32 vcc, v6, v4
	v_add_u32_e32 v7, 1, v3
	s_nop 0
	v_cndmask_b32_e32 v3, v3, v7, vcc
	v_sub_u32_e32 v7, v6, v4
	v_cndmask_b32_e32 v6, v6, v7, vcc
	v_cmp_ge_u32_e32 vcc, v6, v4
	v_add_u32_e32 v6, 1, v3
	s_nop 0
	v_cndmask_b32_e32 v3, v3, v6, vcc
	v_add_u32_e32 v6, 1, v5
	v_mad_u64_u32 v[4:5], s[6:7], v4, v3, v[4:5]
	v_cmp_ne_u32_e32 vcc, v6, v4
	v_mov_b32_e32 v20, 0
	s_cbranch_vccnz .Lxbar2_nl
	buffer_wbl2 sc1
	buffer_inv sc1
	s_waitcnt vmcnt(1)
	s_sub_u32 s6, s27, s4
	s_lshr_b32 s6, s6, 6
	s_add_u32 s10, s4, 0x2400
	s_addc_u32 s11, s5, 0
	s_add_u32 s10, s10, s6
	s_addc_u32 s11, s11, 0
	global_atomic_add v20, v1, s[10:11]
	s_branch .Lxbar2_poll

; __device__ __forceinline__ unsigned xb_ld(unsigned* p)              { return __hip_atomic_load(p, __ATOMIC_RELAXED, __HIP_MEMORY_SCOPE_AGENT); }
; __device__ __forceinline__ unsigned xb_add(unsigned* p, unsigned v) { return __hip_atomic_fetch_add(p, v, __ATOMIC_RELAXED, __HIP_MEMORY_SCOPE_AGENT); }
; #define XB_SPIN(cond, bar) do { unsigned _sp = 0; while (cond) { __builtin_amdgcn_s_sleep(1); \
;     if ((++_sp & 255u) == 0u) { if (xb_ld(&(bar)[XB_TMO])) break; if (_sp > XB_SPIN_CAP) { atomicAdd(&(bar)[XB_TMO], 1u); break; } } } } while (0)
; __device__ __forceinline__ void xcd_barrier(const XcdBarrier& b) {
;     ...
;     if (b.w0 == 0 && ln_ == 0) {
;         unsigned* bar = b.bar; unsigned one_ = 1u;
;         asm volatile("" : "+s"(bar), "+v"(one_));
;         __builtin_amdgcn_s_waitcnt(0);
;         unsigned nloc = b.st[0], nx = b.st[1];
;         if (nloc == 0u) { xcd_barrier_complete(bar, b.x, nloc, nx); b.st[0] = nloc; b.st[1] = nx; }
;         const unsigned old = xb_add(&bar[XB_XSUB(b.x)], one_);
;         const unsigned gen = old / nloc;
;         if (old + 1u == (gen + 1u) * nloc) {
;             __builtin_amdgcn_fence(__ATOMIC_RELEASE, "agent");
;             asm volatile("s_waitcnt vmcnt(0)" ::: "memory");
;             const unsigned og = xb_add(&bar[XB_TOP], one_);
;             const unsigned tg = og / nx;
;             if (og + 1u == (tg + 1u) * nx) xb_add(&bar[XB_TOPGEN], one_);
;             else XB_SPIN(xb_ld(&bar[XB_TOPGEN]) == tg, bar);
;             __builtin_amdgcn_fence(__ATOMIC_ACQUIRE, "agent");
;             xb_add(&bar[XB_XGEN(b.x)], one_);
;             asm volatile("s_waitcnt vmcnt(0)" ::: "memory");
;         } else {
;             XB_SPIN(xb_ld(&bar[XB_XGEN(b.x)]) == gen, bar);
;             __builtin_amdgcn_fence(__ATOMIC_ACQUIRE, "agent");
;             asm volatile("s_waitcnt vmcnt(0)" ::: "memory");
;         }
.LBB0_928:
	v_readlane_b32 s6, v253, 57
	s_lshl_b32 s6, s6, 2
	s_add_u32 s29, s4, s6
	s_addc_u32 s28, s5, 0
	v_mov_b32_e32 v3, s29
	v_add_co_u32_e32 v6, vcc, 0x1000, v3
	v_mov_b32_e32 v3, s28
	s_nop 0
	v_addc_co_u32_e32 v7, vcc, 0, v3, vcc
	flat_atomic_add v5, v[6:7], v1 offset:1024 sc0
	v_cvt_f32_u32_e32 v3, v4
	v_sub_u32_e32 v6, 0, v4
	v_rcp_iflag_f32_e32 v3, v3
	s_nop 0
	v_mul_f32_e32 v3, 0x4f7ffffe, v3
	v_cvt_u32_f32_e32 v3, v3
	v_mul_lo_u32 v6, v6, v3
	v_mul_hi_u32 v6, v3, v6
	v_add_u32_e32 v3, v3, v6
	s_waitcnt vmcnt(0) lgkmcnt(0)
	v_mul_hi_u32 v3, v5, v3
	v_mul_lo_u32 v6, v3, v4
	v_sub_u32_e32 v6, v5, v6
	v_cmp_ge_u32_e32 vcc, v6, v4
	v_add_u32_e32 v7, 1, v3
	s_nop 0
	v_cndmask_b32_e32 v3, v3, v7, vcc
	v_sub_u32_e32 v7, v6, v4
	v_cndmask_b32_e32 v6, v6, v7, vcc
	v_cmp_ge_u32_e32 vcc, v6, v4
	v_add_u32_e32 v6, 1, v3
	s_nop 0
	v_cndmask_b32_e32 v3, v3, v6, vcc
	v_add_u32_e32 v6, 1, v5
	v_mad_u64_u32 v[4:5], s[6:7], v4, v3, v[4:5]
	v_cmp_ne_u32_e32 vcc, v6, v4
	v_mov_b32_e32 v20, 0
	s_cbranch_vccnz .Lxbar4_nl
	buffer_wbl2 sc1
	buffer_inv sc1
	s_waitcnt vmcnt(1)
	s_sub_u32 s6, s29, s4
	s_lshr_b32 s6, s6, 6
	s_add_u32 s10, s4, 0x2400
	s_addc_u32 s11, s5, 0
	s_add_u32 s10, s10, s6
	s_addc_u32 s11, s11, 0
	global_atomic_add v20, v1, s[10:11]
	s_branch .Lxbar4_poll

; __device__ __forceinline__ unsigned xb_ld(unsigned* p)              { return __hip_atomic_load(p, __ATOMIC_RELAXED, __HIP_MEMORY_SCOPE_AGENT); }
; __device__ __forceinline__ unsigned xb_add(unsigned* p, unsigned v) { return __hip_atomic_fetch_add(p, v, __ATOMIC_RELAXED, __HIP_MEMORY_SCOPE_AGENT); }
; #define XB_SPIN(cond, bar) do { unsigned _sp = 0; while (cond) { __builtin_amdgcn_s_sleep(1); \
;     if ((++_sp & 255u) == 0u) { if (xb_ld(&(bar)[XB_TMO])) break; if (_sp > XB_SPIN_CAP) { atomicAdd(&(bar)[XB_TMO], 1u); break; } } } } while (0)
; __device__ __forceinline__ void xcd_barrier(const XcdBarrier& b) {
;     ...
;     if (b.w0 == 0 && ln_ == 0) {
;         unsigned* bar = b.bar; unsigned one_ = 1u;
;         asm volatile("" : "+s"(bar), "+v"(one_));
;         __builtin_amdgcn_s_waitcnt(0);
;         unsigned nloc = b.st[0], nx = b.st[1];
;         if (nloc == 0u) { xcd_barrier_complete(bar, b.x, nloc, nx); b.st[0] = nloc; b.st[1] = nx; }
;         const unsigned old = xb_add(&bar[XB_XSUB(b.x)], one_);
;         const unsigned gen = old / nloc;
;         if (old + 1u == (gen + 1u) * nloc) {
;             __builtin_amdgcn_fence(__ATOMIC_RELEASE, "agent");
;             asm volatile("s_waitcnt vmcnt(0)" ::: "memory");
;             const unsigned og = xb_add(&bar[XB_TOP], one_);
;             const unsigned tg = og / nx;
;             if (og + 1u == (tg + 1u) * nx) xb_add(&bar[XB_TOPGEN], one_);
;             else XB_SPIN(xb_ld(&bar[XB_TOPGEN]) == tg, bar);
;             __builtin_amdgcn_fence(__ATOMIC_ACQUIRE, "agent");
;             xb_add(&bar[XB_XGEN(b.x)], one_);
;             asm volatile("s_waitcnt vmcnt(0)" ::: "memory");
;         } else {
;             XB_SPIN(xb_ld(&bar[XB_XGEN(b.x)]) == gen, bar);
;             __builtin_amdgcn_fence(__ATOMIC_ACQUIRE, "agent");
;             asm volatile("s_waitcnt vmcnt(0)" ::: "memory");
;         }
.LBB0_1016:
	v_readlane_b32 s4, v253, 57
	s_lshl_b32 s4, s4, 2
	s_add_u32 s27, s2, s4
	s_addc_u32 s26, s3, 0
	v_mov_b32_e32 v3, s27
	v_add_co_u32_e32 v6, vcc, 0x1000, v3
	v_mov_b32_e32 v3, s26
	s_nop 0
	v_addc_co_u32_e32 v7, vcc, 0, v3, vcc
	flat_atomic_add v5, v[6:7], v1 offset:1024 sc0
	v_cvt_f32_u32_e32 v3, v4
	v_sub_u32_e32 v6, 0, v4
	v_rcp_iflag_f32_e32 v3, v3
	s_nop 0
	v_mul_f32_e32 v3, 0x4f7ffffe, v3
	v_cvt_u32_f32_e32 v3, v3
	v_mul_lo_u32 v6, v6, v3
	v_mul_hi_u32 v6, v3, v6
	v_add_u32_e32 v3, v3, v6
	s_waitcnt vmcnt(0) lgkmcnt(0)
	v_mul_hi_u32 v3, v5, v3
	v_mul_lo_u32 v6, v3, v4
	v_sub_u32_e32 v6, v5, v6
	v_cmp_ge_u32_e32 vcc, v6, v4
	v_add_u32_e32 v7, 1, v3
	s_nop 0
	v_cndmask_b32_e32 v3, v3, v7, vcc
	v_sub_u32_e32 v7, v6, v4
	v_cndmask_b32_e32 v6, v6, v7, vcc
	v_cmp_ge_u32_e32 vcc, v6, v4
	v_add_u32_e32 v6, 1, v3
	s_nop 0
	v_cndmask_b32_e32 v3, v3, v6, vcc
	v_add_u32_e32 v6, 1, v5
	v_mad_u64_u32 v[4:5], s[4:5], v4, v3, v[4:5]
	v_cmp_ne_u32_e32 vcc, v6, v4
	v_mov_b32_e32 v20, 0
	s_cbranch_vccnz .Lxbar5_nl
	buffer_wbl2 sc1
	buffer_inv sc1
	s_waitcnt vmcnt(1)
	s_sub_u32 s4, s27, s2
	s_lshr_b32 s4, s4, 6
	s_add_u32 s8, s2, 0x2400
	s_addc_u32 s9, s3, 0
	s_add_u32 s8, s8, s4
	s_addc_u32 s9, s9, 0
	global_atomic_add v20, v1, s[8:9]
	s_branch .Lxbar5_poll
